# P2 inner loop: next key tile's K fragments read from LDS right after the current S MFMAs (under the softmax arithmetic) instead of at the top of the next iteration
# baseline (speedup 1.0000x reference)
.LBB0_323:
	s_ashr_i32 s7, s7, 2
	s_and_b64 s[8:9], s[86:87], exec
	s_cselect_b32 s57, 0, s7
	s_add_i32 s7, s22, s3
	s_add_i32 s8, s7, -4
	s_cmp_gt_i32 s7, 4
	s_cselect_b32 s8, s8, 0
	v_mov_b32_e32 v81, 0
	s_cmp_gt_i32 s8, s7
	s_cbranch_scc1 .LBB0_337
	s_max_i32 s70, s7, 4
	s_lshl_b32 s29, s57, 7
	s_lshl_b32 s30, s70, 5
	s_add_i32 s8, s30, s29
	v_add_u32_e32 v3, s8, v204
	v_mad_u64_u32 v[192:193], s[8:9], v3, s38, v[186:187]
	s_add_i32 s8, s63, s29
	s_mov_b32 s26, s12
	s_mov_b32 s27, s12
	s_add_i32 s8, s8, s30
	v_mov_b32_e32 v16, v2
	v_mov_b32_e32 v17, v2
	s_mov_b32 s13, s12
	s_mov_b32 s14, s12
	s_mov_b32 s15, s12
	s_mov_b32 s16, s12
	s_mov_b32 s17, s12
	s_mov_b32 s18, s12
	s_mov_b32 s19, s12
	s_mov_b32 s20, s12
	s_mov_b32 s21, s12
	s_mov_b32 s22, s12
	s_mov_b32 s23, s12
	s_mov_b32 s24, s12
	s_mov_b32 s25, s12
	s_lshl_b32 s8, s8, 7
	v_mov_b32_e32 v3, v2
	v_mov_b32_e32 v4, v2
	v_mov_b32_e32 v5, v2
	v_mov_b32_e32 v6, v2
	v_mov_b32_e32 v7, v2
	v_mov_b32_e32 v8, v2
	v_mov_b32_e32 v9, v2
	v_mov_b32_e32 v10, v2
	v_mov_b32_e32 v11, v2
	v_mov_b32_e32 v12, v2
	v_mov_b32_e32 v13, v2
	v_mov_b32_e32 v14, v2
	v_mov_b32_e32 v15, v2
	v_mov_b64_e32 v[64:65], s[26:27]
	v_mov_b64_e32 v[80:81], v[16:17]
	v_mov_b64_e32 v[96:97], v[16:17]
	s_add_i32 s69, s7, 4
	v_add_u32_e32 v193, s8, v202
	v_add_u32_e32 v206, s8, v203
	v_mov_b64_e32 v[62:63], s[24:25]
	v_mov_b64_e32 v[60:61], s[22:23]
	v_mov_b64_e32 v[58:59], s[20:21]
	v_mov_b64_e32 v[56:57], s[18:19]
	v_mov_b64_e32 v[54:55], s[16:17]
	v_mov_b64_e32 v[52:53], s[14:15]
	v_mov_b64_e32 v[50:51], s[12:13]
	v_mov_b64_e32 v[78:79], v[14:15]
	v_mov_b64_e32 v[76:77], v[12:13]
	v_mov_b64_e32 v[74:75], v[10:11]
	v_mov_b64_e32 v[72:73], v[8:9]
	v_mov_b64_e32 v[70:71], v[6:7]
	v_mov_b64_e32 v[68:69], v[4:5]
	v_mov_b64_e32 v[66:67], v[2:3]
	v_mov_b64_e32 v[94:95], v[14:15]
	v_mov_b64_e32 v[92:93], v[12:13]
	v_mov_b64_e32 v[90:91], v[10:11]
	v_mov_b64_e32 v[88:89], v[8:9]
	v_mov_b64_e32 v[86:87], v[6:7]
	v_mov_b64_e32 v[84:85], v[4:5]
	v_mov_b64_e32 v[82:83], v[2:3]
	v_add_u32_e32 v3, 0, v192
	ds_read_b128 v[178:181], v3
	ds_read_b128 v[174:177], v3 offset:16
	ds_read_b128 v[170:173], v3 offset:32
	ds_read_b128 v[166:169], v3 offset:48
.LBB0_325:
	v_add_u32_e32 v3, 0, v206
	ds_read_b64_tr_b16 v[162:163], v3 offset:55296
	ds_read_b64_tr_b16 v[164:165], v3 offset:56320
	ds_read_b64_tr_b16 v[4:5], v3 offset:57344
	ds_read_b64_tr_b16 v[6:7], v3 offset:58368
	v_add_u32_e32 v3, 0, v193
	ds_read_b64_tr_b16 v[12:13], v3 offset:55296
	ds_read_b64_tr_b16 v[14:15], v3 offset:56320
	ds_read_b64_tr_b16 v[8:9], v3 offset:57344
	ds_read_b64_tr_b16 v[10:11], v3 offset:58368
	s_cmp_lg_u32 s69, s70
	s_mov_b64 s[8:9], -1
	s_cbranch_scc0 .LBB0_331
	s_cmp_lg_u32 s7, s70
	s_cbranch_scc0 .LBB0_328
	s_mov_b64 s[8:9], 0
	s_waitcnt lgkmcnt(11)
	v_mfma_f32_32x32x16_bf16 v[98:113], v[178:181], v[138:141], 0

.LBB0_333:
	s_waitcnt lgkmcnt(10)
	v_mfma_f32_32x32x16_bf16 v[98:113], v[174:177], v[142:145], v[98:113]
	s_waitcnt lgkmcnt(9)
	v_mfma_f32_32x32x16_bf16 v[98:113], v[170:173], v[146:149], v[98:113]
	s_waitcnt lgkmcnt(8)
	v_mfma_f32_32x32x16_bf16 v[98:113], v[166:169], v[150:153], v[98:113]
	s_nop 11
	ds_read_b128 v[178:181], v192 offset:4608
	ds_read_b128 v[174:177], v192 offset:4624
	ds_read_b128 v[170:173], v192 offset:4640
	ds_read_b128 v[166:169], v192 offset:4656
	v_max_f32_e32 v3, v99, v99
	v_max_f32_e32 v16, v98, v98
	v_max_f32_e32 v3, v16, v3
	v_max3_f32 v3, v3, v100, v101
	v_max3_f32 v3, v3, v102, v103
	v_max3_f32 v3, v3, v104, v105
	v_max3_f32 v3, v3, v106, v107
	v_max3_f32 v3, v3, v108, v109
	v_max3_f32 v3, v3, v110, v111
	v_max3_f32 v3, v3, v112, v113
	v_mov_b32_e32 v16, v3
	s_nop 1
	v_permlane32_swap_b32_e32 v3, v16
	v_max_f32_e32 v16, v16, v16
	v_max_f32_e32 v3, v3, v3
	v_max_f32_e32 v3, v3, v16
	v_add_f32_e32 v16, 0x41000000, v205
	v_cmp_gt_f32_e32 vcc, v3, v16
	s_cbranch_vccz .LBB0_335
	v_max_f32_e32 v3, v3, v3
	v_max_f32_e32 v16, v205, v205
	v_max_f32_e32 v3, v16, v3
	v_sub_f32_e32 v16, v205, v3
	v_exp_f32_e32 v16, v16
	v_mov_b32_e32 v205, v3
	v_mul_f32_e32 v50, v50, v16
	v_pk_mul_f32 v[80:81], v[80:81], v[16:17] op_sel_hi:[1,0]
	v_pk_mul_f32 v[78:79], v[78:79], v[16:17] op_sel_hi:[1,0]
	v_pk_mul_f32 v[76:77], v[76:77], v[16:17] op_sel_hi:[1,0]
	v_pk_mul_f32 v[74:75], v[74:75], v[16:17] op_sel_hi:[1,0]
	v_pk_mul_f32 v[72:73], v[72:73], v[16:17] op_sel_hi:[1,0]
	v_pk_mul_f32 v[70:71], v[70:71], v[16:17] op_sel_hi:[1,0]
	v_pk_mul_f32 v[68:69], v[68:69], v[16:17] op_sel_hi:[1,0]
	v_pk_mul_f32 v[66:67], v[66:67], v[16:17] op_sel_hi:[1,0]
	v_pk_mul_f32 v[96:97], v[96:97], v[16:17] op_sel_hi:[1,0]
	v_pk_mul_f32 v[94:95], v[94:95], v[16:17] op_sel_hi:[1,0]
	v_pk_mul_f32 v[92:93], v[92:93], v[16:17] op_sel_hi:[1,0]
	v_pk_mul_f32 v[90:91], v[90:91], v[16:17] op_sel_hi:[1,0]
	v_pk_mul_f32 v[88:89], v[88:89], v[16:17] op_sel_hi:[1,0]
	v_pk_mul_f32 v[86:87], v[86:87], v[16:17] op_sel_hi:[1,0]
	v_pk_mul_f32 v[84:85], v[84:85], v[16:17] op_sel_hi:[1,0]
	v_pk_mul_f32 v[82:83], v[82:83], v[16:17] op_sel_hi:[1,0]
